# P1 as well: descriptor and address setup of stages 2-7 hoisted out of the load segments into the previous MFMA run
# baseline (speedup 1.0000x reference)
.LBB2_34:
	ds_read_b128 v[144:147], v203
	ds_read_b128 v[148:151], v203 offset:2048
	ds_read_b128 v[156:159], v204
	ds_read_b128 v[152:155], v204 offset:2048
	s_cmp_lg_u32 s74, 12
	s_cselect_b64 s[0:1], -1, 0
	s_and_b64 s[4:5], s[0:1], exec
	s_cselect_b32 s75, s73, s68
	s_cselect_b32 s16, s72, s69
	s_mov_b32 m0, s53
	s_and_b32 s5, s71, 0xffff
	s_mov_b32 s4, s70
	ds_read_b128 v[184:187], v205
	ds_read_b128 v[172:175], v205 offset:2048
	ds_read_b128 v[188:191], v206
	ds_read_b128 v[176:179], v206 offset:2048
	ds_read_b128 v[168:171], v205 offset:4096
	ds_read_b128 v[160:163], v205 offset:6144
	ds_read_b128 v[180:183], v206 offset:4096
	ds_read_b128 v[164:167], v206 offset:6144
	buffer_load_dwordx4 v193, s[4:7], 0 offen lds
	s_mov_b32 m0, s54
	s_or_b64 s[36:37], s[28:29], s[0:1]
	buffer_load_dwordx4 v197, s[4:7], 0 offen lds
	s_waitcnt lgkmcnt(8)
	s_barrier
	s_waitcnt lgkmcnt(0)
	s_setprio 1
	v_mfma_i32_16x16x64_i8 v[124:127], v[144:147], v[184:187], v[124:127]
	s_xor_b64 s[34:35], s[36:37], -1
	s_and_b32 s17, s75, 0xffff
	v_mfma_i32_16x16x64_i8 v[120:123], v[148:151], v[184:187], v[120:123]
	s_mov_b32 s18, s6
	s_mov_b32 s19, s7
	v_mfma_i32_16x16x64_i8 v[108:111], v[144:147], v[172:175], v[108:111]
	v_mfma_i32_16x16x64_i8 v[104:107], v[148:151], v[172:175], v[104:107]
	v_mfma_i32_16x16x64_i8 v[96:99], v[144:147], v[168:171], v[96:99]
	v_mfma_i32_16x16x64_i8 v[88:91], v[148:151], v[168:171], v[88:91]
	v_mfma_i32_16x16x64_i8 v[80:83], v[144:147], v[160:163], v[80:83]
	v_mfma_i32_16x16x64_i8 v[72:75], v[148:151], v[160:163], v[72:75]
	v_mfma_i32_16x16x64_i8 v[124:127], v[156:159], v[188:191], v[124:127]
	v_mfma_i32_16x16x64_i8 v[120:123], v[152:155], v[188:191], v[120:123]
	v_mfma_i32_16x16x64_i8 v[108:111], v[156:159], v[176:179], v[108:111]
	v_mfma_i32_16x16x64_i8 v[104:107], v[152:155], v[176:179], v[104:107]
	v_mfma_i32_16x16x64_i8 v[96:99], v[156:159], v[180:183], v[96:99]
	v_mfma_i32_16x16x64_i8 v[88:91], v[152:155], v[180:183], v[88:91]
	v_mfma_i32_16x16x64_i8 v[80:83], v[156:159], v[164:167], v[80:83]
	v_mfma_i32_16x16x64_i8 v[72:75], v[152:155], v[164:167], v[72:75]
	s_setprio 0
	s_barrier
	ds_read_b128 v[128:131], v207
	ds_read_b128 v[132:135], v207 offset:2048
	ds_read_b128 v[140:143], v208
	ds_read_b128 v[136:139], v208 offset:2048
	s_and_b64 vcc, exec, s[34:35]
	s_cbranch_vccnz .LBB2_36
	s_mov_b32 m0, s39
	s_nop 0
	buffer_load_dwordx4 v196, s[16:19], 0 offen lds
	s_mov_b32 m0, s40
	s_nop 0
	buffer_load_dwordx4 v198, s[16:19], 0 offen lds
.LBB2_36:
	s_add_u32 s4, s70, 0xfffc0080
	s_addc_u32 s5, s71, -1
	s_barrier
	s_waitcnt lgkmcnt(0)
	s_setprio 1
	v_mfma_i32_16x16x64_i8 v[116:119], v[128:131], v[184:187], v[116:119]
	s_and_b64 s[0:1], s[0:1], exec
	s_cselect_b32 s17, s5, s66
	s_cselect_b32 s4, s4, s67
	v_mfma_i32_16x16x64_i8 v[112:115], v[132:135], v[184:187], v[112:115]
	s_and_b32 s5, s17, 0xffff
	v_mfma_i32_16x16x64_i8 v[100:103], v[128:131], v[172:175], v[100:103]
	v_mfma_i32_16x16x64_i8 v[92:95], v[132:135], v[172:175], v[92:95]
	v_mfma_i32_16x16x64_i8 v[84:87], v[128:131], v[168:171], v[84:87]
	v_mfma_i32_16x16x64_i8 v[76:79], v[132:135], v[168:171], v[76:79]
	v_mfma_i32_16x16x64_i8 v[68:71], v[128:131], v[160:163], v[68:71]
	v_mfma_i32_16x16x64_i8 v[64:67], v[132:135], v[160:163], v[64:67]
	v_mfma_i32_16x16x64_i8 v[116:119], v[140:143], v[188:191], v[116:119]
	v_mfma_i32_16x16x64_i8 v[112:115], v[136:139], v[188:191], v[112:115]
	v_mfma_i32_16x16x64_i8 v[100:103], v[140:143], v[176:179], v[100:103]
	v_mfma_i32_16x16x64_i8 v[92:95], v[136:139], v[176:179], v[92:95]
	v_mfma_i32_16x16x64_i8 v[84:87], v[140:143], v[180:183], v[84:87]
	v_mfma_i32_16x16x64_i8 v[76:79], v[136:139], v[180:183], v[76:79]
	v_mfma_i32_16x16x64_i8 v[68:71], v[140:143], v[164:167], v[68:71]
	v_mfma_i32_16x16x64_i8 v[64:67], v[136:139], v[164:167], v[64:67]
	s_setprio 0
	s_barrier
	ds_read_b128 v[184:187], v205 offset:16384
	ds_read_b128 v[172:175], v205 offset:18432
	ds_read_b128 v[188:191], v206 offset:16384
	ds_read_b128 v[176:179], v206 offset:18432
	ds_read_b128 v[168:171], v205 offset:20480
	ds_read_b128 v[160:163], v205 offset:22528
	ds_read_b128 v[180:183], v206 offset:20480
	ds_read_b128 v[164:167], v206 offset:22528
	v_cndmask_b32_e64 v194, 0, 1, s[36:37]
	v_cmp_ne_u32_e64 s[0:1], 1, v194
	s_andn2_b64 vcc, exec, s[36:37]
	s_cbranch_vccnz .LBB2_38
	s_mov_b32 m0, s38
	s_nop 0
	buffer_load_dwordx4 v193, s[4:7], 0 offen lds
	s_mov_b32 m0, s41
	s_nop 0
	buffer_load_dwordx4 v197, s[4:7], 0 offen lds
.LBB2_38:
	s_barrier
	s_waitcnt lgkmcnt(0)
	s_setprio 1
	v_mfma_i32_16x16x64_i8 v[60:63], v[144:147], v[184:187], v[60:63]
	s_add_u32 s76, s16, 0x4000
	s_addc_u32 s5, s75, 0
	v_mfma_i32_16x16x64_i8 v[56:59], v[148:151], v[184:187], v[56:59]
	s_and_b32 s77, s5, 0xffff
	s_mov_b32 s78, s6
	v_mfma_i32_16x16x64_i8 v[52:55], v[144:147], v[172:175], v[52:55]
	s_mov_b32 s79, s7
	v_mfma_i32_16x16x64_i8 v[44:47], v[148:151], v[172:175], v[44:47]
	v_mfma_i32_16x16x64_i8 v[36:39], v[144:147], v[168:171], v[36:39]
	v_mfma_i32_16x16x64_i8 v[28:31], v[148:151], v[168:171], v[28:31]
	v_mfma_i32_16x16x64_i8 v[20:23], v[144:147], v[160:163], v[20:23]
	v_mfma_i32_16x16x64_i8 v[12:15], v[148:151], v[160:163], v[12:15]
	v_mfma_i32_16x16x64_i8 v[60:63], v[156:159], v[188:191], v[60:63]
	v_mfma_i32_16x16x64_i8 v[56:59], v[152:155], v[188:191], v[56:59]
	v_mfma_i32_16x16x64_i8 v[52:55], v[156:159], v[176:179], v[52:55]
	v_mfma_i32_16x16x64_i8 v[44:47], v[152:155], v[176:179], v[44:47]
	v_mfma_i32_16x16x64_i8 v[36:39], v[156:159], v[180:183], v[36:39]
	v_mfma_i32_16x16x64_i8 v[28:31], v[152:155], v[180:183], v[28:31]
	v_mfma_i32_16x16x64_i8 v[20:23], v[156:159], v[164:167], v[20:23]
	v_mfma_i32_16x16x64_i8 v[12:15], v[152:155], v[164:167], v[12:15]
	s_setprio 0
	s_barrier
	s_mov_b64 s[18:19], -1
	s_and_b64 vcc, exec, s[34:35]
	s_cbranch_vccz .LBB2_40
	s_waitcnt vmcnt(0)
	s_mov_b64 s[18:19], 0
.LBB2_40:
	s_andn2_b64 vcc, exec, s[18:19]
	s_cbranch_vccnz .LBB2_42
	s_mov_b32 m0, s42
	s_nop 0
	buffer_load_dwordx4 v196, s[76:79], 0 offen lds
	s_mov_b32 m0, s43
	s_nop 0
	buffer_load_dwordx4 v198, s[76:79], 0 offen lds
	s_waitcnt vmcnt(6)
.LBB2_42:
	s_barrier
	s_setprio 1
	v_mfma_i32_16x16x64_i8 v[48:51], v[128:131], v[184:187], v[48:51]
	s_add_i32 s5, 0, 0x18000
	v_add_u32_e32 v210, s5, v199
	v_mfma_i32_16x16x64_i8 v[40:43], v[132:135], v[184:187], v[40:43]
	v_add_u32_e32 v211, s5, v200
	v_mfma_i32_16x16x64_i8 v[32:35], v[128:131], v[172:175], v[32:35]
	s_add_u32 s76, s4, 0x40000
	s_addc_u32 s5, s17, 0
	v_mfma_i32_16x16x64_i8 v[24:27], v[132:135], v[172:175], v[24:27]
	s_and_b32 s77, s5, 0xffff
	s_mov_b32 s78, s6
	v_mfma_i32_16x16x64_i8 v[16:19], v[128:131], v[168:171], v[16:19]
	s_mov_b32 s79, s7
	v_mfma_i32_16x16x64_i8 v[8:11], v[132:135], v[168:171], v[8:11]
	v_mfma_i32_16x16x64_i8 v[4:7], v[128:131], v[160:163], v[4:7]
	v_mfma_i32_16x16x64_i8 v[0:3], v[132:135], v[160:163], v[0:3]
	v_mfma_i32_16x16x64_i8 v[48:51], v[140:143], v[188:191], v[48:51]
	v_mfma_i32_16x16x64_i8 v[40:43], v[136:139], v[188:191], v[40:43]
	v_mfma_i32_16x16x64_i8 v[32:35], v[140:143], v[176:179], v[32:35]
	v_mfma_i32_16x16x64_i8 v[24:27], v[136:139], v[176:179], v[24:27]
	v_mfma_i32_16x16x64_i8 v[16:19], v[140:143], v[180:183], v[16:19]
	v_mfma_i32_16x16x64_i8 v[8:11], v[136:139], v[180:183], v[8:11]
	v_mfma_i32_16x16x64_i8 v[4:7], v[140:143], v[164:167], v[4:7]
	v_mfma_i32_16x16x64_i8 v[0:3], v[136:139], v[164:167], v[0:3]
	s_setprio 0
	s_barrier
	ds_read_b128 v[128:131], v210
	ds_read_b128 v[132:135], v210 offset:2048
	ds_read_b128 v[140:143], v211
	ds_read_b128 v[136:139], v211 offset:2048
	ds_read_b128 v[184:187], v205 offset:32768
	ds_read_b128 v[172:175], v205 offset:34816
	ds_read_b128 v[188:191], v206 offset:32768
	ds_read_b128 v[176:179], v206 offset:34816
	ds_read_b128 v[168:171], v205 offset:36864
	ds_read_b128 v[160:163], v205 offset:38912
	ds_read_b128 v[180:183], v206 offset:36864
	ds_read_b128 v[164:167], v206 offset:38912
	s_and_b64 vcc, exec, s[0:1]
	s_cbranch_vccnz .LBB2_44
	s_mov_b32 m0, s44
	s_nop 0
	buffer_load_dwordx4 v193, s[76:79], 0 offen lds
	s_mov_b32 m0, s45
	s_nop 0
	buffer_load_dwordx4 v197, s[76:79], 0 offen lds
.LBB2_44:
	s_waitcnt lgkmcnt(8)
	s_barrier
	s_waitcnt lgkmcnt(0)
	s_setprio 1
	v_mfma_i32_16x16x64_i8 v[124:127], v[128:131], v[184:187], v[124:127]
	s_add_u32 s76, s16, 0x80
	s_addc_u32 s5, s75, 0
	v_mfma_i32_16x16x64_i8 v[120:123], v[132:135], v[184:187], v[120:123]
	s_and_b32 s77, s5, 0xffff
	s_mov_b32 s78, s6
	v_mfma_i32_16x16x64_i8 v[108:111], v[128:131], v[172:175], v[108:111]
	s_mov_b32 s79, s7
	v_mfma_i32_16x16x64_i8 v[104:107], v[132:135], v[172:175], v[104:107]
	v_mfma_i32_16x16x64_i8 v[96:99], v[128:131], v[168:171], v[96:99]
	v_mfma_i32_16x16x64_i8 v[88:91], v[132:135], v[168:171], v[88:91]
	v_mfma_i32_16x16x64_i8 v[80:83], v[128:131], v[160:163], v[80:83]
	v_mfma_i32_16x16x64_i8 v[72:75], v[132:135], v[160:163], v[72:75]
	v_mfma_i32_16x16x64_i8 v[124:127], v[140:143], v[188:191], v[124:127]
	v_mfma_i32_16x16x64_i8 v[120:123], v[136:139], v[188:191], v[120:123]
	v_mfma_i32_16x16x64_i8 v[108:111], v[140:143], v[176:179], v[108:111]
	v_mfma_i32_16x16x64_i8 v[104:107], v[136:139], v[176:179], v[104:107]
	v_mfma_i32_16x16x64_i8 v[96:99], v[140:143], v[180:183], v[96:99]
	v_mfma_i32_16x16x64_i8 v[88:91], v[136:139], v[180:183], v[88:91]
	v_mfma_i32_16x16x64_i8 v[80:83], v[140:143], v[164:167], v[80:83]
	v_mfma_i32_16x16x64_i8 v[72:75], v[136:139], v[164:167], v[72:75]
	s_setprio 0
	s_barrier
	ds_read_b128 v[144:147], v212
	ds_read_b128 v[148:151], v212 offset:2048
	ds_read_b128 v[156:159], v213
	ds_read_b128 v[152:155], v213 offset:2048
	s_and_b64 vcc, exec, s[0:1]
	s_cbranch_vccnz .LBB2_46
	s_mov_b32 m0, s47
	s_nop 0
	buffer_load_dwordx4 v196, s[76:79], 0 offen lds
	s_mov_b32 m0, s48
	s_nop 0
	buffer_load_dwordx4 v198, s[76:79], 0 offen lds
.LBB2_46:
	s_barrier
	s_waitcnt lgkmcnt(0)
	s_setprio 1
	v_mfma_i32_16x16x64_i8 v[116:119], v[144:147], v[184:187], v[116:119]
	s_add_u32 s4, s4, 0x80
	s_addc_u32 s5, s17, 0
	v_mfma_i32_16x16x64_i8 v[112:115], v[148:151], v[184:187], v[112:115]
	s_and_b32 s5, s5, 0xffff
	v_mfma_i32_16x16x64_i8 v[100:103], v[144:147], v[172:175], v[100:103]
	v_mfma_i32_16x16x64_i8 v[92:95], v[148:151], v[172:175], v[92:95]
	v_mfma_i32_16x16x64_i8 v[84:87], v[144:147], v[168:171], v[84:87]
	v_mfma_i32_16x16x64_i8 v[76:79], v[148:151], v[168:171], v[76:79]
	v_mfma_i32_16x16x64_i8 v[68:71], v[144:147], v[160:163], v[68:71]
	v_mfma_i32_16x16x64_i8 v[64:67], v[148:151], v[160:163], v[64:67]
	v_mfma_i32_16x16x64_i8 v[116:119], v[156:159], v[188:191], v[116:119]
	v_mfma_i32_16x16x64_i8 v[112:115], v[152:155], v[188:191], v[112:115]
	v_mfma_i32_16x16x64_i8 v[100:103], v[156:159], v[176:179], v[100:103]
	v_mfma_i32_16x16x64_i8 v[92:95], v[152:155], v[176:179], v[92:95]
	v_mfma_i32_16x16x64_i8 v[84:87], v[156:159], v[180:183], v[84:87]
	v_mfma_i32_16x16x64_i8 v[76:79], v[152:155], v[180:183], v[76:79]
	v_mfma_i32_16x16x64_i8 v[68:71], v[156:159], v[164:167], v[68:71]
	v_mfma_i32_16x16x64_i8 v[64:67], v[152:155], v[164:167], v[64:67]
	s_setprio 0
	s_barrier
	ds_read_b128 v[184:187], v205 offset:49152
	ds_read_b128 v[172:175], v205 offset:51200
	ds_read_b128 v[188:191], v206 offset:49152
	ds_read_b128 v[176:179], v206 offset:51200
	ds_read_b128 v[168:171], v205 offset:53248
	ds_read_b128 v[160:163], v205 offset:55296
	ds_read_b128 v[180:183], v206 offset:53248
	ds_read_b128 v[164:167], v206 offset:55296
	s_and_b64 vcc, exec, s[0:1]
	s_cbranch_vccnz .LBB2_48
	s_mov_b32 m0, s49
	s_nop 0
	buffer_load_dwordx4 v193, s[4:7], 0 offen lds
	s_mov_b32 m0, s50
	s_nop 0
	buffer_load_dwordx4 v197, s[4:7], 0 offen lds
